# code placement: LSTM loop head shifted by one nop to a 4-mod-8 byte phase
# speedup vs baseline: 1.0011x; 1.0011x over previous
_Z12lstm2_kernelPKDF16_PKDv8_DF16_Pf:
	s_load_dwordx4 s[8:11], s[0:1], 0x0
	s_load_dwordx2 s[12:13], s[0:1], 0x10
	s_and_b32 s14, s2, 1
	s_lshr_b32 s15, s2, 1
	v_and_b32_e32 v1, 63, v0
	v_lshrrev_b32_e32 v2, 6, v0
	v_lshrrev_b32_e32 v3, 4, v1
	v_and_b32_e32 v4, 15, v0
	v_lshrrev_b32_e32 v5, 2, v4
	v_and_b32_e32 v6, 3, v0
	v_lshlrev_b32_e32 v7, 4, v1
	v_lshl_add_u32 v8, v2, 13, v7
	v_lshl_add_u32 v9, v2, 14, v7
	s_waitcnt lgkmcnt(0)
	s_lshl_b32 s16, s14, 15
	s_add_u32 s16, s16, 0x64000
	s_add_u32 s16, s10, s16
	s_addc_u32 s17, s11, 0
	s_lshl_b32 s18, s14, 16
	s_add_u32 s18, s18, 0x44000
	s_add_u32 s18, s10, s18
	s_addc_u32 s19, s11, 0
	v_add_u32_e32 v10, 0x1000, v8
	global_load_dwordx4 v[16:19], v8, s[16:17] offset:0
	global_load_dwordx4 v[20:23], v8, s[16:17] offset:1024
	global_load_dwordx4 v[24:27], v8, s[16:17] offset:2048
	global_load_dwordx4 v[28:31], v8, s[16:17] offset:3072
	global_load_dwordx4 v[32:35], v10, s[16:17] offset:0
	global_load_dwordx4 v[36:39], v10, s[16:17] offset:1024
	global_load_dwordx4 v[40:43], v10, s[16:17] offset:2048
	global_load_dwordx4 v[44:47], v10, s[16:17] offset:3072
	v_add_u32_e32 v11, 0x1000, v9
	v_add_u32_e32 v12, 0x2000, v9
	v_add_u32_e32 v13, 0x3000, v9
	global_load_dwordx4 v[48:51], v9, s[18:19] offset:0
	global_load_dwordx4 v[52:55], v9, s[18:19] offset:1024
	global_load_dwordx4 v[56:59], v9, s[18:19] offset:2048
	global_load_dwordx4 v[60:63], v9, s[18:19] offset:3072
	global_load_dwordx4 v[64:67], v11, s[18:19] offset:0
	global_load_dwordx4 v[68:71], v11, s[18:19] offset:1024
	global_load_dwordx4 v[72:75], v11, s[18:19] offset:2048
	global_load_dwordx4 v[76:79], v11, s[18:19] offset:3072
	global_load_dwordx4 v[80:83], v12, s[18:19] offset:0
	global_load_dwordx4 v[84:87], v12, s[18:19] offset:1024
	global_load_dwordx4 v[88:91], v12, s[18:19] offset:2048
	global_load_dwordx4 v[92:95], v12, s[18:19] offset:3072
	global_load_dwordx4 v[96:99], v13, s[18:19] offset:0
	global_load_dwordx4 v[100:103], v13, s[18:19] offset:1024
	global_load_dwordx4 v[104:107], v13, s[18:19] offset:2048
	global_load_dwordx4 v[108:111], v13, s[18:19] offset:3072
	s_lshl_b32 s22, s14, 10
	s_add_u32 s22, s8, s22
	s_addc_u32 s23, s9, 0
	v_lshl_add_u32 v14, v2, 4, v3
	v_lshlrev_b32_e32 v14, 2, v14
	global_load_dword v112, v14, s[22:23] offset:0
	global_load_dword v113, v14, s[22:23] offset:256
	global_load_dword v114, v14, s[22:23] offset:512
	global_load_dword v115, v14, s[22:23] offset:768
	global_load_dword v116, v14, s[22:23] offset:16
	global_load_dword v117, v14, s[22:23] offset:272
	global_load_dword v118, v14, s[22:23] offset:528
	global_load_dword v119, v14, s[22:23] offset:784
	global_load_dword v120, v14, s[22:23] offset:32
	global_load_dword v121, v14, s[22:23] offset:288
	global_load_dword v122, v14, s[22:23] offset:544
	global_load_dword v123, v14, s[22:23] offset:800
	global_load_dword v124, v14, s[22:23] offset:48
	global_load_dword v125, v14, s[22:23] offset:304
	global_load_dword v126, v14, s[22:23] offset:560
	global_load_dword v127, v14, s[22:23] offset:816
	s_add_u32 s24, s8, 0xc808000
	s_addc_u32 s25, s9, 0
	s_lshl_b32 s26, s15, 2
	v_add_u32_e32 v15, s26, v6
	s_cmp_eq_u32 s14, 0
	v_sub_u32_e32 v200, 0x18f, v5
	s_cselect_b64 vcc, -1, 0
	s_nop 1
	v_cndmask_b32_e32 v200, v200, v5, vcc
	v_mov_b32_e32 v201, 0x190
	v_mad_u32_u24 v200, v15, v201, v200
	v_lshlrev_b32_e32 v200, 8, v200
	v_lshl_add_u32 v200, v3, 4, v200
	v_mov_b32_e32 v201, 0
	v_lshl_add_u64 v[228:229], s[24:25], 0, v[200:201]
	s_mov_b32 s28, 0x400
	s_cselect_b32 s20, s28, 0xfffffc00
	s_cselect_b32 s21, 0, -1
	global_load_dwordx4 v[128:131], v[228:229], off offset:0
	global_load_dwordx4 v[132:135], v[228:229], off offset:64
	global_load_dwordx4 v[136:139], v[228:229], off offset:128
	global_load_dwordx4 v[140:143], v[228:229], off offset:192
	v_lshl_add_u64 v[228:229], v[228:229], 0, s[20:21]
	global_load_dwordx4 v[144:147], v[228:229], off offset:0
	global_load_dwordx4 v[148:151], v[228:229], off offset:64
	global_load_dwordx4 v[152:155], v[228:229], off offset:128
	global_load_dwordx4 v[156:159], v[228:229], off offset:192
	v_lshl_add_u64 v[228:229], v[228:229], 0, s[20:21]
	v_mul_u32_u24_e32 v202, 144, v6
	v_lshl_add_u32 v224, v3, 4, v202
	v_lshl_add_u32 v203, v2, 4, v3
	v_lshl_add_u32 v203, v5, 2, v203
	v_lshl_add_u32 v225, v203, 1, v202
	v_mul_u32_u24_e32 v204, 8704, v2
	v_lshlrev_b32_e32 v205, 8, v3
	v_lshl_add_u32 v205, v6, 4, v205
	v_add_u32_e32 v205, 1280, v205
	v_add_u32_e32 v205, v205, v204
	v_lshl_add_u32 v226, v5, 6, v205
	v_mul_u32_u24_e32 v206, 1088, v5
	v_add_u32_e32 v227, v205, v206
	v_lshlrev_b32_e32 v206, 4, v3
	v_cmp_gt_u32_e32 vcc, 2, v5
	s_nop 1
	v_add_u32_e32 v208, 1152, v206
	v_cndmask_b32_e32 v209, v208, v224, vcc
	v_cndmask_b32_e32 v211, v224, v208, vcc
	v_add_u32_e32 v208, 576, v206
	v_cndmask_b32_e32 v210, v208, v224, vcc
	v_cndmask_b32_e32 v212, v224, v208, vcc
	s_lshl_b32 s27, s14, 6
	v_lshl_add_u32 v230, v15, 7, v203
	v_add_u32_e32 v230, s27, v230
	v_lshlrev_b32_e32 v230, 2, v230
	v_mov_b32_e32 v208, 0
	v_lshlrev_b32_e32 v200, 2, v0
	v_lshlrev_b32_e32 v201, 2, v1
	ds_write_b32 v200, v208
	ds_write_b32 v201, v208 offset:1024
	v_mov_b32_e32 v220, 0
	v_mov_b32_e32 v221, 0xff61b1e6
	v_mov_b32_e32 v222, 0x4038aa3b
	v_mov_b32_e32 v215, 0xff61b1e6
	s_waitcnt vmcnt(0)
	v_mfma_f32_16x16x32_f16 v[168:171], v[48:51], v[128:131], v[112:115]
	v_mfma_f32_16x16x32_f16 v[168:171], v[52:55], v[132:135], v[168:171]
	v_mfma_f32_16x16x32_f16 v[168:171], v[56:59], v[136:139], v[168:171]
	v_mfma_f32_16x16x32_f16 v[168:171], v[60:63], v[140:143], v[168:171]
	v_mfma_f32_16x16x32_f16 v[172:175], v[64:67], v[128:131], v[116:119]
	v_mfma_f32_16x16x32_f16 v[172:175], v[68:71], v[132:135], v[172:175]
	v_mfma_f32_16x16x32_f16 v[172:175], v[72:75], v[136:139], v[172:175]
	v_mfma_f32_16x16x32_f16 v[172:175], v[76:79], v[140:143], v[172:175]
	v_mfma_f32_16x16x32_f16 v[176:179], v[80:83], v[128:131], v[120:123]
	v_mfma_f32_16x16x32_f16 v[176:179], v[84:87], v[132:135], v[176:179]
	v_mfma_f32_16x16x32_f16 v[176:179], v[88:91], v[136:139], v[176:179]
	v_mfma_f32_16x16x32_f16 v[176:179], v[92:95], v[140:143], v[176:179]
	v_mfma_f32_16x16x32_f16 v[180:183], v[96:99], v[128:131], v[124:127]
	v_mfma_f32_16x16x32_f16 v[180:183], v[100:103], v[132:135], v[180:183]
	v_mfma_f32_16x16x32_f16 v[180:183], v[104:107], v[136:139], v[180:183]
	v_mfma_f32_16x16x32_f16 v[180:183], v[108:111], v[140:143], v[180:183]
	v_mfma_f32_16x16x32_f16 v[160:163], v[48:51], v[144:147], v[112:115]
	v_mfma_f32_16x16x32_f16 v[164:167], v[64:67], v[144:147], v[116:119]
	v_mfma_f32_16x16x32_f16 v[160:163], v[52:55], v[148:151], v[160:163]
	v_mfma_f32_16x16x32_f16 v[160:163], v[56:59], v[152:155], v[160:163]
	s_nop 7
	ds_write_b128 v227, v[168:171] offset:0
	ds_write_b128 v227, v[172:175] offset:64
	ds_write_b128 v227, v[176:179] offset:128
	ds_write_b128 v227, v[180:183] offset:192
	global_load_dwordx4 v[128:131], v[228:229], off offset:0
	global_load_dwordx4 v[132:135], v[228:229], off offset:64
	global_load_dwordx4 v[136:139], v[228:229], off offset:128
	global_load_dwordx4 v[140:143], v[228:229], off offset:192
	v_lshl_add_u64 v[228:229], v[228:229], 0, s[20:21]
	s_movk_i32 s4, 50
	s_waitcnt lgkmcnt(0)
	s_barrier
	ds_read_b128 v[192:195], v226 offset:0
	s_nop 0
